# LN1 step: the four LDS reads of the router partial sums are issued together with counted waits (same addition order) instead of four dependent round trips
# baseline (speedup 1.0000x reference)
; template <int CTRL> __device__ __forceinline__ float dpp_f(float v) { return __builtin_bit_cast(float, __builtin_amdgcn_update_dpp(0, __builtin_bit_cast(int, v), CTRL, 0xf, 0xf, true)); }
; template <int CTRL> __device__ __forceinline__ int dpp_i(int v) { return __builtin_amdgcn_update_dpp(0, v, CTRL, 0xf, 0xf, true); }
; #define TOPSTEP(OV, OI) do { const float ov = (OV); const int oi = (OI); if (ov > bv || (ov == bv && oi < bi)) { bv = ov; bi = oi; } } while (0)
; __device__ __forceinline__ void ph_ln1_route(CArgs& a, int l, LAS unsigned char* lds, int bid, int nblk) {
;     ...
;         {
;             float cur = bre;
; #pragma unroll
;             for (int ww = 0; ww < 8; ++ww) cur += part[((ww * 2 + (e >> 4)) * 16 + 2 * w + par) * 16 + (e & 15)];
;             float tvv[4]; int ti[4];
; #pragma unroll
;             for (int k = 0; k < 4; ++k) { float bv = cur; int bi = e;
;     ...
;                 TOPSTEP(dpp_f<0xB1>(bv), dpp_i<0xB1>(bi)); TOPSTEP(dpp_f<0x4E>(bv), dpp_i<0x4E>(bi)); TOPSTEP(dpp_f<0x141>(bv), dpp_i<0x141>(bi)); TOPSTEP(dpp_f<0x140>(bv), dpp_i<0x140>(bi));
;                 TOPSTEP(__shfl_xor(bv, 16), __shfl_xor(bi, 16));
;     ...
;                 tvv[k] = bv; ti[k] = bi; if (e == bi) cur = -3.0e38f; }
.LBB0_2952:
	s_waitcnt lgkmcnt(0)
	s_barrier
	s_waitcnt vmcnt(16)
	ds_read2st64_b32 v[100:101], v180 offset1:8
	ds_read2st64_b32 v[210:211], v180 offset0:16 offset1:24
	ds_read2st64_b32 v[212:213], v180 offset0:32 offset1:40
	ds_read2st64_b32 v[214:215], v180 offset0:48 offset1:56
	v_mov_b32_dpp v104, v127 quad_perm:[1,0,3,2] row_mask:0xf bank_mask:0xf bound_ctrl:1
	s_waitcnt lgkmcnt(3)
	v_add_f32_e32 v34, v148, v100
	v_add_f32_e32 v34, v34, v101
	s_waitcnt lgkmcnt(2)
	v_add_f32_e32 v34, v34, v210
	v_add_f32_e32 v34, v34, v211
	s_waitcnt lgkmcnt(1)
	v_add_f32_e32 v34, v34, v212
	v_add_f32_e32 v34, v34, v213
	s_waitcnt lgkmcnt(0)
	v_add_f32_e32 v34, v34, v214
	v_add_f32_e32 v101, v34, v215
	s_nop 1
	v_mov_b32_dpp v103, v101 quad_perm:[1,0,3,2] row_mask:0xf bank_mask:0xf bound_ctrl:1
	v_cmp_lt_f32_e64 s[56:57], v101, v103
	v_cmp_nlt_f32_e32 vcc, v101, v103
	s_and_saveexec_b64 s[58:59], vcc
	v_cmp_eq_f32_e32 vcc, v101, v103
	v_cmp_lt_i32_e64 s[54:55], v104, v127
	s_and_b64 s[18:19], vcc, s[54:55]
	s_andn2_b64 s[20:21], s[56:57], exec
	s_and_b64 s[18:19], s[18:19], exec
	s_or_b64 s[56:57], s[20:21], s[18:19]
	s_or_b64 exec, exec, s[58:59]
	v_mov_b32_e32 v102, v101
	v_mov_b32_e32 v100, v101
	v_mov_b32_e32 v34, v127
	s_and_saveexec_b64 s[54:55], s[56:57]
	v_mov_b32_e32 v102, v103
	v_mov_b32_e32 v100, v103
	v_mov_b32_e32 v34, v104
	s_or_b64 exec, exec, s[54:55]
	v_mov_b32_dpp v103, v102 quad_perm:[2,3,0,1] row_mask:0xf bank_mask:0xf bound_ctrl:1
	v_mov_b32_dpp v104, v34 quad_perm:[2,3,0,1] row_mask:0xf bank_mask:0xf bound_ctrl:1
	v_cmp_lt_f32_e64 s[56:57], v100, v103
	v_cmp_nlt_f32_e32 vcc, v100, v103
	s_and_saveexec_b64 s[58:59], vcc
	v_cmp_eq_f32_e32 vcc, v100, v103
	v_cmp_lt_i32_e64 s[54:55], v104, v34
	s_and_b64 s[18:19], vcc, s[54:55]
	s_andn2_b64 s[20:21], s[56:57], exec
	s_and_b64 s[18:19], s[18:19], exec
	s_or_b64 s[56:57], s[20:21], s[18:19]
	s_or_b64 exec, exec, s[58:59]
	s_and_saveexec_b64 s[54:55], s[56:57]
	v_mov_b32_e32 v102, v103
	v_mov_b32_e32 v100, v103
	v_mov_b32_e32 v34, v104
	s_or_b64 exec, exec, s[54:55]
	v_mov_b32_dpp v103, v102 row_half_mirror row_mask:0xf bank_mask:0xf bound_ctrl:1
	v_mov_b32_dpp v104, v34 row_half_mirror row_mask:0xf bank_mask:0xf bound_ctrl:1
	v_cmp_lt_f32_e64 s[56:57], v100, v103
	v_cmp_nlt_f32_e32 vcc, v100, v103
	s_and_saveexec_b64 s[58:59], vcc
	v_cmp_eq_f32_e32 vcc, v100, v103
	v_cmp_lt_i32_e64 s[54:55], v104, v34
	s_and_b64 s[18:19], vcc, s[54:55]
	s_andn2_b64 s[20:21], s[56:57], exec
	s_and_b64 s[18:19], s[18:19], exec
	s_or_b64 s[56:57], s[20:21], s[18:19]
	s_or_b64 exec, exec, s[58:59]
	s_and_saveexec_b64 s[54:55], s[56:57]
	v_mov_b32_e32 v102, v103
	v_mov_b32_e32 v100, v103
	v_mov_b32_e32 v34, v104
	s_or_b64 exec, exec, s[54:55]
	v_mov_b32_dpp v103, v102 row_mirror row_mask:0xf bank_mask:0xf bound_ctrl:1
	v_mov_b32_dpp v104, v34 row_mirror row_mask:0xf bank_mask:0xf bound_ctrl:1
	v_cmp_lt_f32_e64 s[56:57], v100, v103
	v_cmp_nlt_f32_e32 vcc, v100, v103
	s_and_saveexec_b64 s[58:59], vcc
	v_cmp_eq_f32_e32 vcc, v100, v103
	v_cmp_lt_i32_e64 s[54:55], v104, v34
	s_and_b64 s[18:19], vcc, s[54:55]
	s_andn2_b64 s[20:21], s[56:57], exec
	s_and_b64 s[18:19], s[18:19], exec
	s_or_b64 s[56:57], s[20:21], s[18:19]
	s_or_b64 exec, exec, s[58:59]
	s_and_saveexec_b64 s[54:55], s[56:57]
	v_mov_b32_e32 v102, v103
	v_mov_b32_e32 v100, v103
	v_mov_b32_e32 v34, v104
	s_or_b64 exec, exec, s[54:55]
	ds_bpermute_b32 v102, v152, v102
	ds_bpermute_b32 v103, v152, v34
	s_waitcnt lgkmcnt(1)
	v_cmp_lt_f32_e64 s[56:57], v100, v102
	v_cmp_nlt_f32_e32 vcc, v100, v102
	s_and_saveexec_b64 s[58:59], vcc
	s_cbranch_execz .LBB0_2970
	v_cmp_eq_f32_e32 vcc, v100, v102
	s_waitcnt lgkmcnt(0)
	v_cmp_lt_i32_e64 s[54:55], v103, v34
	s_and_b64 s[18:19], vcc, s[54:55]
	s_andn2_b64 s[20:21], s[56:57], exec
	s_and_b64 s[18:19], s[18:19], exec
	s_or_b64 s[56:57], s[20:21], s[18:19]
